# moe_dn reuses the MoE tile table left in LDS by moe_gu of the same layer instead of rebuilding it from the counts (on top of v46)
# speedup vs baseline: 1.0131x; 1.0021x over previous
.LBB0_1621:
	v_mbcnt_lo_u32_b32 v0, -1, 0
	v_mbcnt_hi_u32_b32 v0, -1, v0
	v_lshl_add_u32 v160, s43, 6, v0
	s_nop 0
	v_readfirstlane_b32 s28, v160
	s_ashr_i32 s6, s28, 6
	s_lshl_b32 s3, s6, 5
	v_lshrrev_b32_e32 v1, 4, v160
	v_bfe_u32 v2, v160, 4, 2
	s_and_b32 s8, s3, 0x60
	s_ashr_i32 s9, s28, 8
	v_and_b32_e32 v0, 15, v160
	v_bfe_u32 v4, v1, 1, 1
	v_lshlrev_b32_e32 v1, 5, v2
	v_lshlrev_b32_e32 v7, 2, v160
	s_lshr_b32 s3, s8, 3
	v_and_b32_e32 v5, 32, v1
	s_lshl_b32 s2, s9, 13
	v_lshlrev_b32_e32 v6, 10, v4
	v_lshlrev_b32_e32 v3, 6, v0
	v_and_b32_e32 v7, 32, v7
	v_or_b32_e32 v4, s3, v4
	v_bitop3_b32 v5, v3, v7, v5 bitop3:0x36
	v_lshlrev_b32_e32 v4, 10, v4
	s_add_i32 s2, s2, 0
	v_readlane_b32 s0, v254, 41
	v_and_b32_e32 v7, 16, v160
	v_add3_u32 v6, s2, v5, v6
	v_add3_u32 v4, s0, v5, v4
	v_bitop3_b32 v5, v160, 16, v160 bitop3:0xc
	v_readlane_b32 s0, v254, 53
	v_mov_b32_e32 v188, 0x7f7f7f7f
	v_add_u32_e32 v189, v7, v6
	v_add_u32_e32 v190, v7, v4
	v_add_u32_e32 v191, v5, v6
	v_add_u32_e32 v192, v5, v4
	v_mov_b32_e32 v4, s0
	s_waitcnt lgkmcnt(0)
	s_barrier
	ds_read_b32 v4, v4
	v_readlane_b32 s2, v253, 62
	v_readlane_b32 s3, v253, 63
	s_and_b64 vcc, exec, s[2:3]
	s_waitcnt lgkmcnt(0)
	v_readfirstlane_b32 s7, v4
	s_cbranch_vccz .LBB0_1646
	s_lshl_b32 s4, s7, 2
	s_cmp_lt_i32 s94, s4
	s_mov_b64 s[2:3], 0
	s_cselect_b64 s[4:5], -1, 0
	s_branch .LBB0_1647
